# v52 + priority 3 while a wave issues its 16 mask-scan loads, back to base priority for the processing
# baseline (speedup 1.0000x reference)
_Z7k_gemm1PKfS0_PKDv4_jPKiPiS6_P15HIP_vector_typeIiLj2EEPDF16_S0_S6_S9_:
	v_lshrrev_b32_e32 v142, 6, v0
	s_mov_b32 s10, s2
	v_readfirstlane_b32 s90, v0
	s_nop 0
	s_mov_b32 s92, 0
	s_cmp_lt_u32 s90, 0x100
	s_cbranch_scc1 .Lg1_prio_done
	s_cmp_ge_u32 s90, 0x200
	s_cbranch_scc1 .Lg1_prio_done
	s_setprio 1
	s_mov_b32 s92, 1

.LBB1_7:
	s_setprio 3
	s_lshl_b32 s24, s41, 10
	v_lshl_add_u64 v[2:3], s[24:25], 4, v[136:137]
	v_add_co_u32_e32 v4, vcc, 0x1000, v2
	global_load_dwordx4 v[126:129], v[2:3], off nt
	global_load_dwordx4 v[122:125], v[2:3], off offset:1024 nt
	global_load_dwordx4 v[118:121], v[2:3], off offset:2048 nt
	global_load_dwordx4 v[114:117], v[2:3], off offset:3072 nt
	v_addc_co_u32_e32 v5, vcc, 0, v3, vcc
	global_load_dwordx4 v[110:113], v[4:5], off nt
	global_load_dwordx4 v[106:109], v[4:5], off offset:1024 nt
	global_load_dwordx4 v[102:105], v[4:5], off offset:2048 nt
	global_load_dwordx4 v[98:101], v[4:5], off offset:3072 nt
	v_add_co_u32_e32 v4, vcc, 0x2000, v2
	v_lshl_or_b32 v138, s41, 12, v143
	s_nop 0
	v_addc_co_u32_e32 v5, vcc, 0, v3, vcc
	v_add_co_u32_e32 v2, vcc, 0x3000, v2
	global_load_dwordx4 v[94:97], v[4:5], off nt
	global_load_dwordx4 v[30:33], v[4:5], off offset:1024 nt
	global_load_dwordx4 v[26:29], v[4:5], off offset:2048 nt
	global_load_dwordx4 v[22:25], v[4:5], off offset:3072 nt
	v_addc_co_u32_e32 v3, vcc, 0, v3, vcc
	global_load_dwordx4 v[14:17], v[2:3], off nt
	global_load_dwordx4 v[10:13], v[2:3], off offset:1024 nt
	global_load_dwordx4 v[6:9], v[2:3], off offset:2048 nt
	s_nop 0
	global_load_dwordx4 v[2:5], v[2:3], off offset:3072 nt
	s_cmp_eq_u32 s92, 1
	s_cbranch_scc1 .Lg1_base1
	s_setprio 0
	s_branch .Lg1_base_done
.Lg1_base1:
	s_setprio 1
.Lg1_base_done:
	s_waitcnt vmcnt(15)
	v_cmp_neq_f32_e64 s[8:9], 0, v126
	v_cmp_neq_f32_e64 s[6:7], 0, v127
	v_cmp_neq_f32_e64 s[4:5], 0, v128
	s_or_b64 s[36:37], s[8:9], s[6:7]
	v_cmp_neq_f32_e64 s[2:3], 0, v129
	s_or_b64 s[36:37], s[4:5], s[36:37]
	s_or_b64 vcc, s[2:3], s[36:37]
	s_cbranch_vccz .LBB1_21
	v_cndmask_b32_e64 v139, 0, 1, s[8:9]
	v_cmp_ne_u32_e32 vcc, 0, v139
	s_and_saveexec_b64 s[36:37], s[8:9]
	s_cbranch_execz .LBB1_11
	v_mbcnt_lo_u32_b32 v139, vcc_lo, 0
	v_mbcnt_hi_u32_b32 v139, vcc_hi, v139
	v_add_u32_e32 v140, s40, v139
	v_cmp_gt_i32_e64 s[8:9], s33, v140
	s_and_b64 exec, exec, s[8:9]
	s_cbranch_execz .LBB1_11
	v_ashrrev_i32_e32 v141, 31, v140
	v_lshl_add_u64 v[140:141], v[140:141], 3, v[134:135]
	v_mov_b32_e32 v139, v126
	global_store_dwordx2 v[140:141], v[138:139], off
